# speedup vs baseline: 1.0228x; 1.0228x over previous
_Z7k_frontPKiS0_PKfPiP15HIP_vector_typeIjLj2EES2_S2_PDF16_S2_S7_:
	s_cmpk_gt_u32 s2, 0x186
	s_mov_b64 s[4:5], -1
	v_lshlrev_b32_e32 v1, 2, v0
	s_cbranch_scc0 .LBB0_4
	s_load_dwordx2 s[4:5], s[0:1], 0x28
	s_load_dwordx4 s[16:19], s[0:1], 0x40
	v_lshlrev_b32_e32 v30, 4, v0
	v_mov_b32_e32 v31, 0
	v_lshrrev_b32_e32 v33, 6, v0
	s_lshl_b32 s20, s2, 3
	s_addk_i32 s20, 0xf3c8
	s_movk_i32 s21, 0x186a
	s_movk_i32 s3, 0x110
	v_or_b32_e32 v2, s20, v33
	v_add_u32_e32 v53, 0x2000, v30
	v_add_u32_e32 v54, 0x4000, v30
	v_add_u32_e32 v55, 0x6000, v30
	v_cmp_gt_i32_e64 s[22:23], s21, v2
	s_waitcnt lgkmcnt(0)
	global_load_dwordx4 v[56:59], v30, s[4:5]
	global_load_dwordx4 v[60:63], v53, s[4:5]
	global_load_dwordx4 v[64:67], v54, s[4:5]
	global_load_dwordx4 v[68:71], v55, s[4:5]
	v_min_i32_e32 v2, 0x1869, v2
	v_lshlrev_b32_e32 v32, 4, v2
	v_bfe_u32 v40, v0, 5, 1
	v_and_b32_e32 v2, 31, v0
	v_or_b32_e32 v36, v32, v40
	v_lshlrev_b32_e32 v2, 4, v2
	v_mov_b32_e32 v3, v31
	v_ashrrev_i32_e32 v37, 31, v36
	s_waitcnt lgkmcnt(0)
	v_lshl_add_u64 v[34:35], s[16:17], 0, v[2:3]
	v_lshlrev_b64 v[2:3], 9, v[36:37]
	v_lshl_add_u64 v[10:11], v[34:35], 0, v[2:3]
	v_or_b32_e32 v2, 2, v36
	v_ashrrev_i32_e32 v3, 31, v2
	v_lshlrev_b64 v[2:3], 9, v[2:3]
	v_lshl_add_u64 v[12:13], v[34:35], 0, v[2:3]
	global_load_dwordx4 v[6:9], v[10:11], off nt
	global_load_dwordx4 v[2:5], v[12:13], off nt
	v_or_b32_e32 v10, 4, v36
	v_ashrrev_i32_e32 v11, 31, v10
	v_lshlrev_b64 v[10:11], 9, v[10:11]
	v_lshl_add_u64 v[18:19], v[34:35], 0, v[10:11]
	v_or_b32_e32 v10, 6, v36
	v_ashrrev_i32_e32 v11, 31, v10
	v_lshlrev_b64 v[10:11], 9, v[10:11]
	v_lshl_add_u64 v[20:21], v[34:35], 0, v[10:11]
	global_load_dwordx4 v[14:17], v[18:19], off nt
	global_load_dwordx4 v[10:13], v[20:21], off nt
	v_or_b32_e32 v18, 8, v36
	v_ashrrev_i32_e32 v19, 31, v18
	v_lshlrev_b64 v[18:19], 9, v[18:19]
	v_lshl_add_u64 v[26:27], v[34:35], 0, v[18:19]
	v_or_b32_e32 v18, 10, v36
	v_ashrrev_i32_e32 v19, 31, v18
	v_lshlrev_b64 v[18:19], 9, v[18:19]
	v_lshl_add_u64 v[28:29], v[34:35], 0, v[18:19]
	global_load_dwordx4 v[22:25], v[26:27], off nt
	global_load_dwordx4 v[18:21], v[28:29], off nt
	v_or_b32_e32 v26, 12, v36
	v_or_b32_e32 v36, 14, v36
	v_ashrrev_i32_e32 v27, 31, v26
	v_ashrrev_i32_e32 v37, 31, v36
	v_lshlrev_b64 v[26:27], 9, v[26:27]
	v_lshlrev_b64 v[36:37], 9, v[36:37]
	v_lshl_add_u64 v[26:27], v[34:35], 0, v[26:27]
	v_lshl_add_u64 v[34:35], v[34:35], 0, v[36:37]
	global_load_dwordx4 v[26:29], v[26:27], off nt
	v_and_b32_e32 v41, 0x7c, v1
	global_load_dwordx4 v[36:39], v[34:35], off nt
	v_and_b32_e32 v53, 15, v0
	v_mul_u32_u24_e32 v53, 0x440, v53
	v_lshrrev_b32_e32 v54, 4, v0
	v_lshl_add_u32 v53, v54, 1, v53
	s_waitcnt vmcnt(8)
	v_cvt_f16_f32_e32 v56, v56
	v_cvt_f16_f32_e32 v57, v57
	v_cvt_f16_f32_e32 v58, v58
	v_cvt_f16_f32_e32 v59, v59
	v_cvt_f16_f32_e32 v60, v60
	v_cvt_f16_f32_e32 v61, v61
	v_cvt_f16_f32_e32 v62, v62
	v_cvt_f16_f32_e32 v63, v63
	v_cvt_f16_f32_e32 v64, v64
	v_cvt_f16_f32_e32 v65, v65
	v_cvt_f16_f32_e32 v66, v66
	v_cvt_f16_f32_e32 v67, v67
	v_cvt_f16_f32_e32 v68, v68
	v_cvt_f16_f32_e32 v69, v69
	v_cvt_f16_f32_e32 v70, v70
	v_cvt_f16_f32_e32 v71, v71
	ds_write_b16 v53, v56
	ds_write_b16 v53, v57 offset:272
	ds_write_b16 v53, v58 offset:544
	ds_write_b16 v53, v59 offset:816
	ds_write_b16 v53, v60 offset:64
	ds_write_b16 v53, v61 offset:336
	ds_write_b16 v53, v62 offset:608
	ds_write_b16 v53, v63 offset:880
	ds_write_b16 v53, v64 offset:128
	ds_write_b16 v53, v65 offset:400
	ds_write_b16 v53, v66 offset:672
	ds_write_b16 v53, v67 offset:944
	ds_write_b16 v53, v68 offset:192
	ds_write_b16 v53, v69 offset:464
	ds_write_b16 v53, v70 offset:736
	ds_write_b16 v53, v71 offset:1008
	s_waitcnt lgkmcnt(0)
	s_barrier
	s_and_saveexec_b64 s[8:9], s[22:23]
	s_cbranch_execz .LBB0_3
	v_mul_u32_u24_e32 v34, 0x1100, v33
	v_lshrrev_b32_e32 v42, 1, v0
	v_lshl_or_b32 v41, v41, 1, v34
	v_and_b32_e32 v52, 24, v42
	v_and_b32_e32 v35, 15, v0
	v_mad_u32_u24 v40, v40, s3, v41
	v_lshlrev_b32_e32 v41, 1, v52
	v_add_u32_e32 v42, 0x4000, v40
	v_mad_u32_u24 v48, v35, s3, v41
	v_add_u32_e32 v43, 0x4800, v40
	v_add_u32_e32 v40, 0x5000, v40
	s_movk_i32 s4, 0x1100
	v_and_b32_e32 v30, 0x70, v30
	s_waitcnt vmcnt(7)
	v_cvt_pk_f16_f32 v9, v8, v9
	v_cvt_pk_f16_f32 v8, v6, v7
	s_waitcnt vmcnt(6)
	v_cvt_pk_f16_f32 v5, v4, v5
	v_cvt_pk_f16_f32 v4, v2, v3
	s_waitcnt vmcnt(5)
	v_cvt_pk_f16_f32 v3, v16, v17
	v_cvt_pk_f16_f32 v2, v14, v15
	s_waitcnt vmcnt(4)
	v_cvt_pk_f16_f32 v7, v12, v13
	v_cvt_pk_f16_f32 v6, v10, v11
	s_waitcnt vmcnt(3)
	v_cvt_pk_f16_f32 v11, v24, v25
	v_cvt_pk_f16_f32 v10, v22, v23
	s_waitcnt vmcnt(2)
	v_cvt_pk_f16_f32 v13, v20, v21
	v_cvt_pk_f16_f32 v12, v18, v19
	s_waitcnt vmcnt(1)
	v_cvt_pk_f16_f32 v15, v28, v29
	v_cvt_pk_f16_f32 v14, v26, v27
	s_waitcnt vmcnt(0)
	v_cvt_pk_f16_f32 v17, v38, v39
	v_cvt_pk_f16_f32 v16, v36, v37
	ds_write2_b64 v42, v[8:9], v[4:5] offset0:128 offset1:196
	ds_write2_b64 v43, v[2:3], v[6:7] offset0:8 offset1:76
	ds_write2_b64 v43, v[10:11], v[12:13] offset0:144 offset1:212
	ds_write2_b64 v40, v[14:15], v[16:17] offset0:24 offset1:92
	s_waitcnt lgkmcnt(0)
	ds_read_b128 v[2:5], v48
	v_mul_u32_u24_e32 v6, 0x110, v35
	v_mad_u32_u24 v33, v33, s4, v6
	v_add_u32_e32 v35, v33, v41
	ds_read_b128 v[6:9], v35 offset:17408
	ds_read_b128 v[10:13], v35 offset:17472
	ds_read_b128 v[14:17], v48 offset:64
	ds_read_b128 v[18:21], v48 offset:4352
	ds_read_b128 v[22:25], v48 offset:4416
	s_waitcnt lgkmcnt(4)
	v_mfma_f32_16x16x32_f16 v[2:5], v[2:5], v[6:9], 0
	ds_read_b128 v[26:29], v48 offset:8704
	ds_read_b128 v[36:39], v48 offset:8768
	ds_read_b128 v[40:43], v48 offset:13056
	ds_read_b128 v[44:47], v48 offset:13120
	s_waitcnt lgkmcnt(5)
	v_mfma_f32_16x16x32_f16 v[18:21], v[18:21], v[6:9], 0
	v_mfma_f32_16x16x32_f16 v[2:5], v[14:17], v[10:13], v[2:5]
	s_waitcnt lgkmcnt(4)
	v_mfma_f32_16x16x32_f16 v[14:17], v[22:25], v[10:13], v[18:21]
	ds_read_b128 v[22:25], v48 offset:128
	s_waitcnt lgkmcnt(4)
	v_mfma_f32_16x16x32_f16 v[26:29], v[26:29], v[6:9], 0
	s_waitcnt lgkmcnt(2)
	v_mfma_f32_16x16x32_f16 v[6:9], v[40:43], v[6:9], 0
	v_mfma_f32_16x16x32_f16 v[18:21], v[36:39], v[10:13], v[26:29]
	s_waitcnt lgkmcnt(1)
	v_mfma_f32_16x16x32_f16 v[6:9], v[44:47], v[10:13], v[6:9]
	ds_read_b128 v[10:13], v35 offset:17536
	s_nop 1
	ds_read_b128 v[26:29], v35 offset:17600
	ds_read_b128 v[36:39], v48 offset:192
	s_waitcnt lgkmcnt(2)
	v_mfma_f32_16x16x32_f16 v[2:5], v[22:25], v[10:13], v[2:5]
	ds_read_b128 v[22:25], v48 offset:4480
	ds_read_b128 v[40:43], v48 offset:4544
	s_waitcnt lgkmcnt(1)
	v_mfma_f32_16x16x32_f16 v[14:17], v[22:25], v[10:13], v[14:17]
	ds_read_b128 v[22:25], v48 offset:8832
	ds_read_b128 v[44:47], v48 offset:8896
	s_waitcnt lgkmcnt(1)
	v_mfma_f32_16x16x32_f16 v[18:21], v[22:25], v[10:13], v[18:21]
	ds_read_b128 v[22:25], v48 offset:13184
	ds_read_b128 v[48:51], v48 offset:13248
	s_waitcnt lgkmcnt(0)
	v_mfma_f32_16x16x32_f16 v[6:9], v[22:25], v[10:13], v[6:9]
	v_mfma_f32_16x16x32_f16 v[2:5], v[36:39], v[26:29], v[2:5]
	v_mfma_f32_16x16x32_f16 v[10:13], v[40:43], v[26:29], v[14:17]
	v_mfma_f32_16x16x32_f16 v[14:17], v[44:47], v[26:29], v[18:21]
	s_nop 5
	v_cvt_pk_f16_f32 v5, v4, v5
	v_cvt_pk_f16_f32 v4, v2, v3
	v_cvt_pk_f16_f32 v3, v12, v13
	v_mfma_f32_16x16x32_f16 v[6:9], v[48:51], v[26:29], v[6:9]
	v_add_u32_e32 v18, v33, v52
	v_cvt_pk_f16_f32 v2, v10, v11
	v_add_u32_e32 v10, 0x4000, v18
	ds_write2_b64 v10, v[4:5], v[2:3] offset0:128 offset1:132
	v_cvt_pk_f16_f32 v3, v16, v17
	v_cvt_pk_f16_f32 v2, v14, v15
	s_nop 1
	v_cvt_pk_f16_f32 v5, v8, v9
	v_cvt_pk_f16_f32 v4, v6, v7
	ds_write2_b64 v10, v[2:3], v[4:5] offset0:136 offset1:140
	v_bfe_u32 v6, v0, 3, 3
	v_or_b32_e32 v2, v34, v30
	v_mad_u32_u24 v8, v6, s3, v2
	s_waitcnt lgkmcnt(0)
	ds_read_b128 v[2:5], v8 offset:17408
	v_or_b32_e32 v12, v32, v6
	v_ashrrev_i32_e32 v13, 31, v12
	v_lshl_add_u64 v[10:11], s[18:19], 0, v[30:31]
	v_lshlrev_b64 v[6:7], 7, v[12:13]
	v_lshl_add_u64 v[14:15], v[10:11], 0, v[6:7]
	ds_read_b128 v[6:9], v8 offset:19584
	s_waitcnt lgkmcnt(1)
	global_store_dwordx4 v[14:15], v[2:5], off
	s_nop 1
	v_or_b32_e32 v2, 8, v12
	v_ashrrev_i32_e32 v3, 31, v2
	v_lshlrev_b64 v[2:3], 7, v[2:3]
	v_lshl_add_u64 v[2:3], v[10:11], 0, v[2:3]
	s_waitcnt lgkmcnt(0)
	global_store_dwordx4 v[2:3], v[6:9], off

	.amdhsa_kernel _Z7k_frontPKiS0_PKfPiP15HIP_vector_typeIjLj2EES2_S2_PDF16_S2_S7_
		.amdhsa_group_segment_fixed_size 52224
		.amdhsa_private_segment_fixed_size 0
		.amdhsa_kernarg_size 80
		.amdhsa_user_sgpr_count 2
		.amdhsa_user_sgpr_dispatch_ptr 0
		.amdhsa_user_sgpr_queue_ptr 0
		.amdhsa_user_sgpr_kernarg_segment_ptr 1
		.amdhsa_user_sgpr_dispatch_id 0
		.amdhsa_user_sgpr_kernarg_preload_length 0
		.amdhsa_user_sgpr_kernarg_preload_offset 0
		.amdhsa_user_sgpr_private_segment_size 0
		.amdhsa_uses_dynamic_stack 0
		.amdhsa_enable_private_segment 0
		.amdhsa_system_sgpr_workgroup_id_x 1
		.amdhsa_system_sgpr_workgroup_id_y 0
		.amdhsa_system_sgpr_workgroup_id_z 0
		.amdhsa_system_sgpr_workgroup_info 0
		.amdhsa_system_vgpr_workitem_id 0
		.amdhsa_next_free_vgpr 76
		.amdhsa_next_free_sgpr 91
		.amdhsa_accum_offset 76
		.amdhsa_reserve_vcc 1
		.amdhsa_float_round_mode_32 0
		.amdhsa_float_round_mode_16_64 0
		.amdhsa_float_denorm_mode_32 3
		.amdhsa_float_denorm_mode_16_64 3
		.amdhsa_dx10_clamp 1
		.amdhsa_ieee_mode 1
		.amdhsa_fp16_overflow 0
		.amdhsa_tg_split 0
		.amdhsa_exception_fp_ieee_invalid_op 0
		.amdhsa_exception_fp_denorm_src 0
		.amdhsa_exception_fp_ieee_div_zero 0
		.amdhsa_exception_fp_ieee_overflow 0
		.amdhsa_exception_fp_ieee_underflow 0
		.amdhsa_exception_fp_ieee_inexact 0
		.amdhsa_exception_int_div_zero 0
	.end_amdhsa_kernel

_Z5k_midPK15HIP_vector_typeIjLj2EEPKiPiPfPjPDF16_:
	s_load_dwordx2 s[4:5], s[0:1], 0x8
	s_load_dwordx2 s[44:45], s[0:1], 0x28
	s_and_b32 s3, s2, 7
	s_lshr_b32 s2, s2, 3
	s_mul_i32 s35, s3, 49
	s_add_i32 s35, s35, s2
	v_min_u32_e32 v1, 0x186, v0
	s_movk_i32 s2, 0x188
	v_mov_b32_e32 v2, s35
	v_mad_u32_u24 v4, v1, s2, v2
	v_mov_b32_e32 v5, 0
	s_waitcnt lgkmcnt(0)
	v_lshl_add_u64 v[2:3], v[4:5], 2, s[4:5]
	global_load_dwordx2 v[2:3], v[2:3], off
	s_lshl_b32 s46, s35, 8
	v_lshrrev_b32_e32 v72, 3, v0
	v_or_b32_e32 v72, s46, v72
	v_and_b32_e32 v56, 7, v0
	v_lshlrev_b32_e32 v56, 4, v56
	v_min_u32_e32 v60, 0x1869f, v72
	v_lshl_or_b32 v60, v60, 7, v56
	v_add_u32_e32 v64, 64, v72
	v_min_u32_e32 v64, 0x1869f, v64
	v_lshl_or_b32 v64, v64, 7, v56
	v_add_u32_e32 v68, 0x80, v72
	v_min_u32_e32 v68, 0x1869f, v68
	v_lshl_or_b32 v68, v68, 7, v56
	v_add_u32_e32 v72, 0xc0, v72
	v_min_u32_e32 v72, 0x1869f, v72
	v_lshl_or_b32 v72, v72, 7, v56
	global_load_dwordx4 v[60:63], v60, s[44:45]
	global_load_dwordx4 v[64:67], v64, s[44:45]
	global_load_dwordx4 v[68:71], v68, s[44:45]
	global_load_dwordx4 v[56:59], v72, s[44:45]
	s_movk_i32 s2, 0x100
	v_cmp_gt_u32_e64 s[4:5], s2, v0
	v_lshlrev_b32_e32 v1, 2, v0
	s_and_saveexec_b64 s[2:3], s[4:5]
	ds_write_b32 v1, v5 offset:3132
	s_or_b64 exec, exec, s[2:3]
	s_movk_i32 s2, 0x187
	v_cmp_gt_u32_e32 vcc, s2, v0
	s_waitcnt vmcnt(4)
	v_sub_u32_e32 v3, v3, v2
	v_and_b32_e32 v7, 63, v0
	v_cndmask_b32_e32 v6, 0, v2, vcc
	v_cndmask_b32_e32 v4, 0, v3, vcc
	v_lshrrev_b32_e32 v20, 6, v0
	v_add_u32_dpp v6, v6, v6 row_shr:1 row_mask:0xf bank_mask:0xf bound_ctrl:1
	v_add_u32_dpp v4, v4, v4 row_shr:1 row_mask:0xf bank_mask:0xf bound_ctrl:1
	v_cmp_eq_u32_e64 s[6:7], 63, v7
	v_add_u32_dpp v6, v6, v6 row_shr:2 row_mask:0xf bank_mask:0xf bound_ctrl:1
	v_add_u32_dpp v4, v4, v4 row_shr:2 row_mask:0xf bank_mask:0xf bound_ctrl:1
	s_nop 0
	v_add_u32_dpp v6, v6, v6 row_shr:4 row_mask:0xf bank_mask:0xf bound_ctrl:1
	v_add_u32_dpp v4, v4, v4 row_shr:4 row_mask:0xf bank_mask:0xf bound_ctrl:1
	s_nop 0
	v_add_u32_dpp v6, v6, v6 row_shr:8 row_mask:0xf bank_mask:0xf bound_ctrl:1
	v_add_u32_dpp v4, v4, v4 row_shr:8 row_mask:0xf bank_mask:0xf bound_ctrl:1
	s_nop 0
	v_add_u32_dpp v6, v6, v6 row_bcast:15 row_mask:0xa bank_mask:0xf
	v_add_u32_dpp v4, v4, v4 row_bcast:15 row_mask:0xa bank_mask:0xf
	s_nop 0
	v_mov_b32_dpp v5, v6 row_bcast:31 row_mask:0xc bank_mask:0xf
	v_add_u32_dpp v4, v4, v4 row_bcast:31 row_mask:0xc bank_mask:0xf
	s_and_saveexec_b64 s[2:3], s[6:7]
	v_add_u32_e32 v5, v6, v5
	v_lshlrev_b32_e32 v6, 2, v20
	v_add_u32_e32 v6, 0x1000, v6
	ds_write2_b32 v6, v4, v5 offset0:15 offset1:23
	s_or_b64 exec, exec, s[2:3]
	v_mov_b32_e32 v5, 0x1074
	s_waitcnt lgkmcnt(0)
	s_barrier
	ds_read2_b32 v[6:7], v5 offset1:1
	v_mov_b32_e32 v5, 0x106c
	v_mov_b32_e32 v10, 0x1064
	v_mov_b32_e32 v12, 0x105c
	ds_read2_b32 v[8:9], v5 offset1:1
	ds_read2_b32 v[10:11], v10 offset1:1
	ds_read2_b32 v[12:13], v12 offset1:1
	v_mov_b32_e32 v5, 0x1054
	s_waitcnt lgkmcnt(3)
	v_readfirstlane_b32 s36, v7
	v_readfirstlane_b32 s38, v6
	s_waitcnt lgkmcnt(1)
	v_readfirstlane_b32 s42, v10
	s_waitcnt lgkmcnt(0)
	v_readfirstlane_b32 s43, v12
	ds_read2_b32 v[6:7], v5 offset1:1
	v_mov_b32_e32 v5, 0x104c
	v_mov_b32_e32 v10, 0x1044
	v_mov_b32_e32 v12, 0x103c
	v_readfirstlane_b32 s39, v9
	v_readfirstlane_b32 s40, v8
	v_readfirstlane_b32 s41, v11
	v_readfirstlane_b32 s37, v13
	ds_read2_b32 v[8:9], v5 offset1:1
	ds_read2_b32 v[10:11], v10 offset1:1
	ds_read2_b32 v[12:13], v12 offset1:1
	s_waitcnt lgkmcnt(3)
	v_readfirstlane_b32 s10, v7
	v_readfirstlane_b32 s11, v6
	s_waitcnt lgkmcnt(2)
	v_readfirstlane_b32 s12, v9
	v_readfirstlane_b32 s13, v8
	s_waitcnt lgkmcnt(1)
	v_readfirstlane_b32 s14, v11
	v_readfirstlane_b32 s15, v10
	s_waitcnt lgkmcnt(0)
	v_readfirstlane_b32 s16, v13
	v_readfirstlane_b32 s17, v12
	s_barrier
	s_and_saveexec_b64 s[2:3], vcc
	s_cbranch_execz .LBB1_6
	s_movk_i32 s8, 0x17f
	v_mov_b32_e32 v5, s12
	v_cmp_lt_u32_e32 vcc, s8, v0
	s_movk_i32 s8, 0x13f
	v_mov_b32_e32 v6, s13
	v_cndmask_b32_e32 v5, 0, v5, vcc
	v_cmp_lt_u32_e32 vcc, s8, v0
	s_movk_i32 s8, 0xff
	v_mov_b32_e32 v7, s14
	v_cndmask_b32_e32 v6, 0, v6, vcc
	v_cmp_lt_u32_e32 vcc, s8, v0
	s_movk_i32 s8, 0xbf
	v_mov_b32_e32 v8, s15
	v_cndmask_b32_e32 v7, 0, v7, vcc
	v_cmp_lt_u32_e32 vcc, s8, v0
	s_movk_i32 s8, 0x7f
	v_mov_b32_e32 v9, s16
	v_cndmask_b32_e32 v8, 0, v8, vcc
	v_cmp_lt_u32_e32 vcc, s8, v0
	v_mov_b32_e32 v10, s17
	v_sub_u32_e32 v3, v4, v3
	v_cndmask_b32_e32 v9, 0, v9, vcc
	v_cmp_lt_u32_e32 vcc, 63, v0
	v_lshl_add_u32 v2, v0, 12, v2
	s_nop 0
	v_cndmask_b32_e32 v10, 0, v10, vcc
	v_add3_u32 v3, v3, v10, v9
	v_add3_u32 v3, v3, v8, v7
	v_add3_u32 v3, v3, v6, v5
	ds_write_b32 v1, v3
	ds_write_b32 v1, v2 offset:1568

.LBB1_30:
	s_cbranch_execz .LBB1_100
	s_max_i32 s10, s33, 1
	s_add_i32 s10, s10, -1
	v_or_b32_e32 v23, 0x200, v0
	v_or_b32_e32 v28, 0x400, v0
	v_or_b32_e32 v22, 0x600, v0
	v_or_b32_e32 v27, 0x800, v0
	v_or_b32_e32 v26, 0xa00, v0
	v_or_b32_e32 v25, 0xc00, v0
	v_or_b32_e32 v24, 0xe00, v0
	v_or_b32_e32 v21, 0x1000, v0
	s_movk_i32 s11, 0x187
	s_mov_b64 s[12:13], exec
	v_cmp_gt_u32_e32 vcc, s11, v0
	s_and_b64 exec, exec, vcc
	s_cbranch_execz .Lmid_fill_done
	ds_read_b32 v2, v1
	ds_read_b32 v3, v1 offset:4
	ds_read_b32 v4, v1 offset:1568
	s_waitcnt lgkmcnt(0)
	v_sub_u32_e32 v3, v3, v2
	v_lshlrev_b32_e32 v2, 2, v2
.Lmid_fill:
	v_cmp_lt_i32_e32 vcc, 0, v3
	s_and_b64 exec, exec, vcc
	s_cbranch_execz .Lmid_fill_done
	ds_write_b32 v2, v4 offset:8192
	v_add_u32_e32 v2, 4, v2
	v_add_u32_e32 v4, 1, v4
	v_add_u32_e32 v3, -1, v3
	s_branch .Lmid_fill
.Lmid_fill_done:
	s_mov_b64 exec, s[12:13]
	s_waitcnt lgkmcnt(0)
	s_barrier
	v_min_u32_e32 v30, s10, v0
	v_min_u32_e32 v31, s10, v23
	v_min_u32_e32 v32, s10, v28
	v_min_u32_e32 v33, s10, v22
	v_min_u32_e32 v34, s10, v27
	v_min_u32_e32 v35, s10, v26
	v_min_u32_e32 v36, s10, v25
	v_min_u32_e32 v37, s10, v24
	v_min_u32_e32 v38, s10, v21
	v_lshlrev_b32_e32 v30, 2, v30
	v_lshlrev_b32_e32 v31, 2, v31
	v_lshlrev_b32_e32 v32, 2, v32
	v_lshlrev_b32_e32 v33, 2, v33
	v_lshlrev_b32_e32 v34, 2, v34
	v_lshlrev_b32_e32 v35, 2, v35
	v_lshlrev_b32_e32 v36, 2, v36
	v_lshlrev_b32_e32 v37, 2, v37
	v_lshlrev_b32_e32 v38, 2, v38
	ds_read_b32 v30, v30 offset:8192
	ds_read_b32 v31, v31 offset:8192
	ds_read_b32 v32, v32 offset:8192
	ds_read_b32 v33, v33 offset:8192
	ds_read_b32 v34, v34 offset:8192
	ds_read_b32 v35, v35 offset:8192
	ds_read_b32 v36, v36 offset:8192
	ds_read_b32 v37, v37 offset:8192
	ds_read_b32 v38, v38 offset:8192
	s_cmp_gt_i32 s33, 0
	s_cselect_b64 vcc, -1, 0
	s_waitcnt lgkmcnt(8)
	v_lshlrev_b32_e32 v30, 3, v30
	v_cndmask_b32_e32 v30, 0, v30, vcc
	global_load_dwordx2 v[18:19], v30, s[8:9]
	s_waitcnt lgkmcnt(7)
	v_lshlrev_b32_e32 v31, 3, v31
	v_cndmask_b32_e32 v31, 0, v31, vcc
	global_load_dwordx2 v[16:17], v31, s[8:9]
	s_waitcnt lgkmcnt(6)
	v_lshlrev_b32_e32 v32, 3, v32
	v_cndmask_b32_e32 v32, 0, v32, vcc
	global_load_dwordx2 v[12:13], v32, s[8:9]
	s_waitcnt lgkmcnt(5)
	v_lshlrev_b32_e32 v33, 3, v33
	v_cndmask_b32_e32 v33, 0, v33, vcc
	global_load_dwordx2 v[8:9], v33, s[8:9]
	s_waitcnt lgkmcnt(4)
	v_lshlrev_b32_e32 v34, 3, v34
	v_cndmask_b32_e32 v34, 0, v34, vcc
	global_load_dwordx2 v[14:15], v34, s[8:9]
	s_waitcnt lgkmcnt(3)
	v_lshlrev_b32_e32 v35, 3, v35
	v_cndmask_b32_e32 v35, 0, v35, vcc
	global_load_dwordx2 v[10:11], v35, s[8:9]
	s_waitcnt lgkmcnt(2)
	v_lshlrev_b32_e32 v36, 3, v36
	v_cndmask_b32_e32 v36, 0, v36, vcc
	global_load_dwordx2 v[6:7], v36, s[8:9]
	s_waitcnt lgkmcnt(1)
	v_lshlrev_b32_e32 v37, 3, v37
	v_cndmask_b32_e32 v37, 0, v37, vcc
	global_load_dwordx2 v[4:5], v37, s[8:9]
	s_waitcnt lgkmcnt(0)
	v_lshlrev_b32_e32 v38, 3, v38
	v_cndmask_b32_e32 v38, 0, v38, vcc
	global_load_dwordx2 v[2:3], v38, s[8:9]
	v_mov_b32_e32 v29, 0
	v_cmp_gt_i32_e32 vcc, s33, v0
	v_mov_b32_e32 v34, 0
	s_waitcnt vmcnt(8)
	v_lshrrev_b32_e32 v31, 15, v18
	s_and_saveexec_b64 s[8:9], vcc
	v_and_b32_e32 v30, 0x1fffc, v31
	v_mov_b32_e32 v32, 1
	ds_add_rtn_u32 v34, v30, v32 offset:3132
	s_or_b64 exec, exec, s[8:9]
	v_cmp_gt_i32_e64 s[8:9], s33, v23
	s_waitcnt vmcnt(7)
	v_lshrrev_b32_e32 v30, 15, v16
	s_and_saveexec_b64 s[10:11], s[8:9]
	v_and_b32_e32 v29, 0x1fffc, v30
	v_mov_b32_e32 v32, 1
	ds_add_rtn_u32 v29, v29, v32 offset:3132
	s_or_b64 exec, exec, s[10:11]
	v_cmp_gt_i32_e64 s[10:11], s33, v28
	v_mov_b32_e32 v28, 0
	s_waitcnt vmcnt(6)
	v_lshrrev_b32_e32 v33, 15, v12
	v_mov_b32_e32 v36, 0
	s_and_saveexec_b64 s[12:13], s[10:11]
	v_and_b32_e32 v32, 0x1fffc, v33
	v_mov_b32_e32 v35, 1
	ds_add_rtn_u32 v36, v32, v35 offset:3132
	s_or_b64 exec, exec, s[12:13]
	v_cmp_gt_i32_e64 s[12:13], s33, v22
	s_waitcnt vmcnt(5)
	v_lshrrev_b32_e32 v32, 15, v8
	s_and_saveexec_b64 s[14:15], s[12:13]
	v_and_b32_e32 v28, 0x1fffc, v32
	v_mov_b32_e32 v35, 1
	ds_add_rtn_u32 v28, v28, v35 offset:3132
	s_or_b64 exec, exec, s[14:15]
	v_cmp_gt_i32_e64 s[14:15], s33, v27
	v_mov_b32_e32 v27, 0
	s_waitcnt vmcnt(4)
	v_lshrrev_b32_e32 v35, 15, v14
	v_mov_b32_e32 v38, 0
	s_and_saveexec_b64 s[16:17], s[14:15]
	v_and_b32_e32 v37, 0x1fffc, v35
	v_mov_b32_e32 v38, 1
	ds_add_rtn_u32 v38, v37, v38 offset:3132
	s_or_b64 exec, exec, s[16:17]
	v_cmp_gt_i32_e64 s[16:17], s33, v26
	s_waitcnt vmcnt(3)
	v_lshrrev_b32_e32 v26, 15, v10
	s_and_saveexec_b64 s[18:19], s[16:17]
	v_and_b32_e32 v27, 0x1fffc, v26
	v_mov_b32_e32 v37, 1
	ds_add_rtn_u32 v27, v27, v37 offset:3132
	s_or_b64 exec, exec, s[18:19]
	v_cmp_gt_i32_e64 s[18:19], s33, v25
	v_mov_b32_e32 v25, 0
	s_waitcnt vmcnt(2)
	v_lshrrev_b32_e32 v37, 15, v6
	v_mov_b32_e32 v40, 0
	s_and_saveexec_b64 s[20:21], s[18:19]
	v_and_b32_e32 v39, 0x1fffc, v37
	v_mov_b32_e32 v40, 1
	ds_add_rtn_u32 v40, v39, v40 offset:3132
	s_or_b64 exec, exec, s[20:21]
	v_cmp_gt_i32_e64 s[20:21], s33, v24
	s_waitcnt vmcnt(1)
	v_lshrrev_b32_e32 v24, 15, v4
	s_and_saveexec_b64 s[22:23], s[20:21]
	v_and_b32_e32 v25, 0x1fffc, v24
	v_mov_b32_e32 v39, 1
	ds_add_rtn_u32 v25, v25, v39 offset:3132
	s_or_b64 exec, exec, s[22:23]
	v_cmp_gt_i32_e64 s[22:23], s33, v21
	v_mov_b32_e32 v42, 0
	s_waitcnt vmcnt(0)
	v_lshrrev_b32_e32 v39, 15, v2
	v_mov_b32_e32 v41, 0
	s_and_saveexec_b64 s[30:31], s[22:23]
	v_and_b32_e32 v21, 0x1fffc, v39
	v_mov_b32_e32 v41, 1
	ds_add_rtn_u32 v41, v21, v41 offset:3132
	s_or_b64 exec, exec, s[30:31]
	s_waitcnt lgkmcnt(0)
	s_barrier
	s_and_saveexec_b64 s[30:31], s[4:5]
	ds_read_b32 v42, v1 offset:3132
	s_or_b64 exec, exec, s[30:31]
	s_waitcnt lgkmcnt(0)
	v_add_u32_dpp v21, v42, v42 row_shr:1 row_mask:0xf bank_mask:0xf bound_ctrl:1
	v_mov_b32_e32 v44, 0
	s_nop 0
	v_add_u32_dpp v21, v21, v21 row_shr:2 row_mask:0xf bank_mask:0xf bound_ctrl:1
	s_nop 1
	v_add_u32_dpp v21, v21, v21 row_shr:4 row_mask:0xf bank_mask:0xf bound_ctrl:1
	s_nop 1
	v_add_u32_dpp v43, v21, v21 row_shr:8 row_mask:0xf bank_mask:0xf bound_ctrl:1
	s_nop 1
	v_add_u32_dpp v43, v43, v43 row_bcast:15 row_mask:0xa bank_mask:0xf
	s_nop 1
	v_add_u32_dpp v43, v43, v43 row_bcast:31 row_mask:0xc bank_mask:0xf
	s_and_saveexec_b64 s[30:31], s[6:7]
	v_lshlrev_b32_e32 v20, 2, v20
	ds_write_b32 v20, v43 offset:4156
	s_or_b64 exec, exec, s[30:31]
	v_mov_b32_e32 v20, 0x103c
	s_waitcnt lgkmcnt(0)
	s_barrier
	ds_read2_b32 v[20:21], v20 offset1:1
	ds_read_b32 v44, v44 offset:4164
	s_waitcnt lgkmcnt(0)
	s_barrier
	s_and_saveexec_b64 s[6:7], s[4:5]
	s_cbranch_execz .LBB1_60
	s_movk_i32 s4, 0xbf
	v_cmp_lt_u32_e64 s[4:5], s4, v0
	v_sub_u32_e32 v42, v43, v42
	s_nop 0
	v_cndmask_b32_e64 v44, 0, v44, s[4:5]
	s_movk_i32 s4, 0x7f
	v_cmp_lt_u32_e64 s[4:5], s4, v0
	s_nop 1
	v_cndmask_b32_e64 v21, 0, v21, s[4:5]
	v_cmp_lt_u32_e64 s[4:5], 63, v0
	s_nop 1
	v_cndmask_b32_e64 v20, 0, v20, s[4:5]
	v_add_u32_e32 v20, v42, v20
	v_add3_u32 v20, v20, v21, v44
	ds_write_b32 v1, v20 offset:3132

.LBB1_100:
	v_lshrrev_b32_e32 v20, 3, v0
	v_and_b32_e32 v1, 7, v0
	v_lshlrev_b32_e32 v1, 4, v1
	v_or_b32_e32 v24, s46, v20
	v_lshlrev_b32_e32 v20, 2, v20
	s_mov_b32 s2, 0x186a0
	s_waitcnt lgkmcnt(0)
	s_barrier
	ds_read_b32 v26, v20 offset:4220
	ds_read_b32 v28, v20 offset:4476
	ds_read_b32 v30, v20 offset:4732
	ds_read_b32 v32, v20 offset:4988
	v_cvt_f32_f16_e32 v2, v60
	v_cvt_f32_f16_sdwa v3, v60 dst_sel:DWORD dst_unused:UNUSED_PAD src0_sel:WORD_1
	v_cvt_f32_f16_e32 v4, v61
	v_cvt_f32_f16_sdwa v5, v61 dst_sel:DWORD dst_unused:UNUSED_PAD src0_sel:WORD_1
	v_cvt_f32_f16_e32 v6, v62
	v_cvt_f32_f16_sdwa v7, v62 dst_sel:DWORD dst_unused:UNUSED_PAD src0_sel:WORD_1
	v_cvt_f32_f16_e32 v8, v63
	v_cvt_f32_f16_sdwa v9, v63 dst_sel:DWORD dst_unused:UNUSED_PAD src0_sel:WORD_1
	v_add_u32_e32 v10, 0, v24
	s_waitcnt lgkmcnt(3)
	v_pk_mul_f32 v[2:3], v[26:27], v[2:3] op_sel_hi:[0,1]
	v_pk_mul_f32 v[4:5], v[26:27], v[4:5] op_sel_hi:[0,1]
	v_pk_mul_f32 v[6:7], v[26:27], v[6:7] op_sel_hi:[0,1]
	v_pk_mul_f32 v[8:9], v[26:27], v[8:9] op_sel_hi:[0,1]
	v_cmp_gt_u32_e32 vcc, s2, v10
	v_lshl_or_b32 v11, v10, 7, v1
	v_cvt_pk_f16_f32 v60, v2, v3
	v_cvt_pk_f16_f32 v61, v4, v5
	v_cvt_pk_f16_f32 v62, v6, v7
	v_cvt_pk_f16_f32 v63, v8, v9
	s_and_saveexec_b64 s[0:1], vcc
	global_store_dwordx4 v11, v[60:63], s[44:45]
	s_or_b64 exec, exec, s[0:1]
	v_cvt_f32_f16_e32 v2, v64
	v_cvt_f32_f16_sdwa v3, v64 dst_sel:DWORD dst_unused:UNUSED_PAD src0_sel:WORD_1
	v_cvt_f32_f16_e32 v4, v65
	v_cvt_f32_f16_sdwa v5, v65 dst_sel:DWORD dst_unused:UNUSED_PAD src0_sel:WORD_1
	v_cvt_f32_f16_e32 v6, v66
	v_cvt_f32_f16_sdwa v7, v66 dst_sel:DWORD dst_unused:UNUSED_PAD src0_sel:WORD_1
	v_cvt_f32_f16_e32 v8, v67
	v_cvt_f32_f16_sdwa v9, v67 dst_sel:DWORD dst_unused:UNUSED_PAD src0_sel:WORD_1
	v_add_u32_e32 v10, 64, v24
	s_waitcnt lgkmcnt(2)
	v_pk_mul_f32 v[2:3], v[28:29], v[2:3] op_sel_hi:[0,1]
	v_pk_mul_f32 v[4:5], v[28:29], v[4:5] op_sel_hi:[0,1]
	v_pk_mul_f32 v[6:7], v[28:29], v[6:7] op_sel_hi:[0,1]
	v_pk_mul_f32 v[8:9], v[28:29], v[8:9] op_sel_hi:[0,1]
	v_cmp_gt_u32_e32 vcc, s2, v10
	v_lshl_or_b32 v11, v10, 7, v1
	v_cvt_pk_f16_f32 v64, v2, v3
	v_cvt_pk_f16_f32 v65, v4, v5
	v_cvt_pk_f16_f32 v66, v6, v7
	v_cvt_pk_f16_f32 v67, v8, v9
	s_and_saveexec_b64 s[0:1], vcc
	global_store_dwordx4 v11, v[64:67], s[44:45]
	s_or_b64 exec, exec, s[0:1]
	v_cvt_f32_f16_e32 v2, v68
	v_cvt_f32_f16_sdwa v3, v68 dst_sel:DWORD dst_unused:UNUSED_PAD src0_sel:WORD_1
	v_cvt_f32_f16_e32 v4, v69
	v_cvt_f32_f16_sdwa v5, v69 dst_sel:DWORD dst_unused:UNUSED_PAD src0_sel:WORD_1
	v_cvt_f32_f16_e32 v6, v70
	v_cvt_f32_f16_sdwa v7, v70 dst_sel:DWORD dst_unused:UNUSED_PAD src0_sel:WORD_1
	v_cvt_f32_f16_e32 v8, v71
	v_cvt_f32_f16_sdwa v9, v71 dst_sel:DWORD dst_unused:UNUSED_PAD src0_sel:WORD_1
	v_add_u32_e32 v10, 0x80, v24
	s_waitcnt lgkmcnt(1)
	v_pk_mul_f32 v[2:3], v[30:31], v[2:3] op_sel_hi:[0,1]
	v_pk_mul_f32 v[4:5], v[30:31], v[4:5] op_sel_hi:[0,1]
	v_pk_mul_f32 v[6:7], v[30:31], v[6:7] op_sel_hi:[0,1]
	v_pk_mul_f32 v[8:9], v[30:31], v[8:9] op_sel_hi:[0,1]
	v_cmp_gt_u32_e32 vcc, s2, v10
	v_lshl_or_b32 v11, v10, 7, v1
	v_cvt_pk_f16_f32 v68, v2, v3
	v_cvt_pk_f16_f32 v69, v4, v5
	v_cvt_pk_f16_f32 v70, v6, v7
	v_cvt_pk_f16_f32 v71, v8, v9
	s_and_saveexec_b64 s[0:1], vcc
	global_store_dwordx4 v11, v[68:71], s[44:45]
	s_or_b64 exec, exec, s[0:1]
	v_cvt_f32_f16_e32 v2, v56
	v_cvt_f32_f16_sdwa v3, v56 dst_sel:DWORD dst_unused:UNUSED_PAD src0_sel:WORD_1
	v_cvt_f32_f16_e32 v4, v57
	v_cvt_f32_f16_sdwa v5, v57 dst_sel:DWORD dst_unused:UNUSED_PAD src0_sel:WORD_1
	v_cvt_f32_f16_e32 v6, v58
	v_cvt_f32_f16_sdwa v7, v58 dst_sel:DWORD dst_unused:UNUSED_PAD src0_sel:WORD_1
	v_cvt_f32_f16_e32 v8, v59
	v_cvt_f32_f16_sdwa v9, v59 dst_sel:DWORD dst_unused:UNUSED_PAD src0_sel:WORD_1
	v_add_u32_e32 v10, 0xc0, v24
	s_waitcnt lgkmcnt(0)
	v_pk_mul_f32 v[2:3], v[32:33], v[2:3] op_sel_hi:[0,1]
	v_pk_mul_f32 v[4:5], v[32:33], v[4:5] op_sel_hi:[0,1]
	v_pk_mul_f32 v[6:7], v[32:33], v[6:7] op_sel_hi:[0,1]
	v_pk_mul_f32 v[8:9], v[32:33], v[8:9] op_sel_hi:[0,1]
	v_cmp_gt_u32_e32 vcc, s2, v10
	v_lshl_or_b32 v11, v10, 7, v1
	v_cvt_pk_f16_f32 v56, v2, v3
	v_cvt_pk_f16_f32 v57, v4, v5
	v_cvt_pk_f16_f32 v58, v6, v7
	v_cvt_pk_f16_f32 v59, v8, v9
	s_and_saveexec_b64 s[0:1], vcc
	global_store_dwordx4 v11, v[56:59], s[44:45]
	s_or_b64 exec, exec, s[0:1]
	s_endpgm

	.amdhsa_kernel _Z5k_midPK15HIP_vector_typeIjLj2EEPKiPiPfPjPDF16_
		.amdhsa_group_segment_fixed_size 45056
		.amdhsa_private_segment_fixed_size 0
		.amdhsa_kernarg_size 48
		.amdhsa_user_sgpr_count 2
		.amdhsa_user_sgpr_dispatch_ptr 0
		.amdhsa_user_sgpr_queue_ptr 0
		.amdhsa_user_sgpr_kernarg_segment_ptr 1
		.amdhsa_user_sgpr_dispatch_id 0
		.amdhsa_user_sgpr_kernarg_preload_length 0
		.amdhsa_user_sgpr_kernarg_preload_offset 0
		.amdhsa_user_sgpr_private_segment_size 0
		.amdhsa_uses_dynamic_stack 0
		.amdhsa_enable_private_segment 0
		.amdhsa_system_sgpr_workgroup_id_x 1
		.amdhsa_system_sgpr_workgroup_id_y 0
		.amdhsa_system_sgpr_workgroup_id_z 0
		.amdhsa_system_sgpr_workgroup_info 0
		.amdhsa_system_vgpr_workitem_id 0
		.amdhsa_next_free_vgpr 76
		.amdhsa_next_free_sgpr 91
		.amdhsa_accum_offset 76
		.amdhsa_reserve_vcc 1
		.amdhsa_float_round_mode_32 0
		.amdhsa_float_round_mode_16_64 0
		.amdhsa_float_denorm_mode_32 3
		.amdhsa_float_denorm_mode_16_64 3
		.amdhsa_dx10_clamp 1
		.amdhsa_ieee_mode 1
		.amdhsa_fp16_overflow 0
		.amdhsa_tg_split 0
		.amdhsa_exception_fp_ieee_invalid_op 0
		.amdhsa_exception_fp_denorm_src 0
		.amdhsa_exception_fp_ieee_div_zero 0
		.amdhsa_exception_fp_ieee_overflow 0
		.amdhsa_exception_fp_ieee_underflow 0
		.amdhsa_exception_fp_ieee_inexact 0
		.amdhsa_exception_int_div_zero 0
	.end_amdhsa_kernel

.LBB2_6:
	s_or_b64 exec, exec, s[6:7]
	v_and_b32_e32 v13, 15, v0
	v_lshlrev_b32_e32 v15, 4, v1
	v_lshlrev_b32_e32 v2, 5, v17
	v_lshrrev_b32_e32 v0, 1, v0
	v_or_b32_e32 v1, v15, v13
	s_waitcnt lgkmcnt(0)
	global_load_dwordx4 v[28:31], v2, s[2:3]
	global_load_dwordx4 v[32:35], v2, s[2:3] offset:16
	v_mov_b32_e32 v9, 0
	v_and_b32_e32 v11, 24, v0
	s_waitcnt vmcnt(3)
	v_lshlrev_b32_e32 v8, 7, v1
	v_lshl_add_u64 v[0:1], s[8:9], 0, v[8:9]
	v_lshlrev_b32_e32 v8, 1, v11
	v_lshl_add_u64 v[36:37], v[0:1], 0, v[8:9]
	global_load_dwordx4 v[4:7], v[36:37], off
	global_load_dwordx4 v[0:3], v[36:37], off offset:64
	s_movk_i32 s2, 0x90
	v_lshlrev_b32_e32 v12, 3, v17
	v_mad_u32_u24 v10, v16, s2, v10
	v_cmp_eq_u32_e32 vcc, 0, v17
	s_waitcnt vmcnt(3)
	v_fma_f32 v19, v18, v19, v28
	v_fma_f32 v20, v18, v20, v29
	v_fma_f32 v21, v18, v21, v30
	v_fmac_f32_e32 v31, v18, v22
	s_waitcnt vmcnt(2)
	v_fma_f32 v22, v18, v23, v32
	v_fma_f32 v23, v18, v24, v33
	v_fma_f32 v24, v18, v25, v34
	v_fmac_f32_e32 v35, v18, v26
	v_max_f32_e32 v19, 0, v19
	v_max_f32_e32 v20, 0, v20
	v_max_f32_e32 v21, 0, v21
	v_max_f32_e32 v25, 0, v31
	v_max_f32_e32 v22, 0, v22
	v_max_f32_e32 v26, 0, v23
	v_max_f32_e32 v23, 0, v24
	v_max_f32_e32 v24, 0, v35
	v_cvt_pk_f16_f32 v23, v23, v24
	v_cvt_pk_f16_f32 v22, v22, v26
	v_cvt_pk_f16_f32 v21, v21, v25
	v_cvt_pk_f16_f32 v20, v19, v20
	ds_write_b128 v10, v[20:23] offset:4608
	s_and_saveexec_b64 s[0:1], vcc
	v_lshlrev_b32_e32 v10, 2, v16
	ds_write_b32 v10, v18 offset:9216
	s_or_b64 exec, exec, s[0:1]
	v_mad_u32_u24 v8, v13, s2, v8
	s_waitcnt lgkmcnt(0)
	s_barrier
	ds_read_b128 v[16:19], v8 offset:4608
	ds_read_b128 v[20:23], v8 offset:4672
	s_waitcnt vmcnt(1) lgkmcnt(1)
	v_mfma_f32_16x16x32_f16 a[0:3], v[4:7], v[16:19], 0
	v_lshlrev_b32_e32 v10, 1, v15
	v_mul_u32_u24_e32 v15, 0x90, v13
	v_lshlrev_b32_e32 v13, 2, v13
	v_add_u32_e32 v13, 0x2400, v13
	ds_read2_b32 v[24:25], v13 offset1:16
	s_waitcnt vmcnt(0) lgkmcnt(1)
	v_mfma_f32_16x16x32_f16 a[0:3], v[0:3], v[20:23], a[0:3]
	ds_read_b128 v[20:23], v8 offset:6976
	s_nop 6
	v_accvgpr_read_b32 v17, a2
	v_accvgpr_read_b32 v16, a1
	s_waitcnt lgkmcnt(1)
	v_pk_mul_f32 v[16:17], v[24:25], v[16:17] op_sel_hi:[0,1]
	v_cvt_pk_f16_f32 v27, v16, v17
	ds_read_b128 v[16:19], v8 offset:6912
	v_accvgpr_read_b32 v13, a0
	v_fma_mixlo_f16 v13, v24, v13, 0
	v_pack_b32_f16 v26, v13, v27
	v_accvgpr_read_b32 v13, a3
	s_waitcnt lgkmcnt(0)
	v_mfma_f32_16x16x32_f16 a[0:3], v[4:7], v[16:19], 0
	v_fma_mixlo_f16 v13, v24, v13, 0
	v_add3_u32 v4, v10, v11, v15
	v_alignbit_b32 v27, v13, v27, 16
	v_mfma_f32_16x16x32_f16 a[0:3], v[0:3], v[20:23], a[0:3]
	ds_write_b64 v4, v[26:27]
	v_add_u32_e32 v8, s12, v14
	s_nop 5
	v_accvgpr_read_b32 v0, a0
	v_fma_mixlo_f16 v5, v25, v0, 0
	v_mov_b32_e32 v0, v25
	v_accvgpr_read_b32 v3, a2
	v_accvgpr_read_b32 v2, a1
	v_pk_mul_f32 v[0:1], v[0:1], v[2:3] op_sel_hi:[0,1]
	v_accvgpr_read_b32 v2, a3
	v_cvt_pk_f16_f32 v1, v0, v1
	v_fma_mixlo_f16 v2, v25, v2, 0
	v_pack_b32_f16 v0, v5, v1
	v_alignbit_b32 v1, v2, v1, 16
	ds_write_b64 v4, v[0:1] offset:2304
	v_mad_u32_u24 v0, v14, s2, v12
	s_waitcnt lgkmcnt(0)
	s_barrier
	ds_read2_b64 v[2:5], v0 offset1:8
	v_lshlrev_b64 v[0:1], 7, v[8:9]
	v_lshl_add_u64 v[0:1], s[10:11], 0, v[0:1]
	v_lshlrev_b32_e32 v8, 1, v12
	v_lshl_add_u64 v[0:1], v[0:1], 0, v[8:9]
	s_waitcnt lgkmcnt(0)
	global_store_dwordx4 v[0:1], v[2:5], off nt
	s_endpgm
	.p2alignl 8, 3212836864

.LBB3_6:
	s_or_b64 exec, exec, s[8:9]
	s_waitcnt lgkmcnt(0)
	global_load_dwordx4 v[0:3], v8, s[2:3]
	global_load_dwordx4 v[18:21], v8, s[2:3] offset:128
	v_lshlrev_b64 v[4:5], 8, v[4:5]
	v_mov_b32_e32 v9, 0
	v_lshl_add_u64 v[4:5], s[6:7], 0, v[4:5]
	v_lshl_add_u64 v[8:9], v[4:5], 0, v[8:9]
	s_waitcnt vmcnt(1)
	v_pk_fma_f32 v[0:1], v[6:7], v[16:17], v[0:1] op_sel_hi:[0,1,1]
	v_pk_fma_f32 v[2:3], v[6:7], v[14:15], v[2:3] op_sel_hi:[0,1,1]
	s_waitcnt vmcnt(0)
	v_pk_fma_f32 v[4:5], v[6:7], v[12:13], v[18:19] op_sel_hi:[0,1,1]
	v_pk_fma_f32 v[6:7], v[6:7], v[10:11], v[20:21] op_sel_hi:[0,1,1]
	global_store_dwordx4 v[8:9], v[0:3], off nt
	global_store_dwordx4 v[8:9], v[4:7], off offset:128 nt
	s_endpgm
	.p2alignl 8, 3212836864

	.text
	.p2alignl 6, 3212836864
	.fill 256, 4, 3212836864
	.p2alignl 8, 3212836864

amdhsa.kernels:
  - .agpr_count:     0
    .args:
      - .actual_access:  read_only
        .address_space:  global
        .offset:         0
        .size:           8
        .value_kind:     global_buffer
      - .actual_access:  read_only
        .address_space:  global
        .offset:         8
        .size:           8
        .value_kind:     global_buffer
      - .actual_access:  read_only
        .address_space:  global
        .offset:         16
        .size:           8
        .value_kind:     global_buffer
      - .actual_access:  write_only
        .address_space:  global
        .offset:         24
        .size:           8
        .value_kind:     global_buffer
      - .actual_access:  write_only
        .address_space:  global
        .offset:         32
        .size:           8
        .value_kind:     global_buffer
      - .actual_access:  read_only
        .address_space:  global
        .offset:         40
        .size:           8
        .value_kind:     global_buffer
      - .actual_access:  read_only
        .address_space:  global
        .offset:         48
        .size:           8
        .value_kind:     global_buffer
      - .actual_access:  write_only
        .address_space:  global
        .offset:         56
        .size:           8
        .value_kind:     global_buffer
      - .actual_access:  read_only
        .address_space:  global
        .offset:         64
        .size:           8
        .value_kind:     global_buffer
      - .actual_access:  write_only
        .address_space:  global
        .offset:         72
        .size:           8
        .value_kind:     global_buffer
    .group_segment_fixed_size: 52224
    .kernarg_segment_align: 8
    .kernarg_segment_size: 80
    .language:       OpenCL C
    .language_version:
      - 2
      - 0
    .max_flat_workgroup_size: 512
    .name:           _Z7k_frontPKiS0_PKfPiP15HIP_vector_typeIjLj2EES2_S2_PDF16_S2_S7_
    .private_segment_fixed_size: 0
    .sgpr_count:     22
    .sgpr_spill_count: 0
    .symbol:         _Z7k_frontPKiS0_PKfPiP15HIP_vector_typeIjLj2EES2_S2_PDF16_S2_S7_.kd
    .uniform_work_group_size: 1
    .uses_dynamic_stack: false
    .vgpr_count:     76
    .vgpr_spill_count: 0
    .wavefront_size: 64
  - .agpr_count:     0
    .args:
      - .actual_access:  read_only
        .address_space:  global
        .offset:         0
        .size:           8
        .value_kind:     global_buffer
      - .actual_access:  read_only
        .address_space:  global
        .offset:         8
        .size:           8
        .value_kind:     global_buffer
      - .actual_access:  write_only
        .address_space:  global
        .offset:         16
        .size:           8
        .value_kind:     global_buffer
      - .actual_access:  write_only
        .address_space:  global
        .offset:         24
        .size:           8
        .value_kind:     global_buffer
      - .actual_access:  write_only
        .address_space:  global
        .offset:         32
        .size:           8
        .value_kind:     global_buffer
      - .address_space:  global
        .offset:         40
        .size:           8
        .value_kind:     global_buffer
    .group_segment_fixed_size: 45056
    .kernarg_segment_align: 8
    .kernarg_segment_size: 48
    .language:       OpenCL C
    .language_version:
      - 2
      - 0
    .max_flat_workgroup_size: 512
    .name:           _Z5k_midPK15HIP_vector_typeIjLj2EEPKiPiPfPjPDF16_
    .private_segment_fixed_size: 0
    .sgpr_count:     50
    .sgpr_spill_count: 0
    .symbol:         _Z5k_midPK15HIP_vector_typeIjLj2EEPKiPiPfPjPDF16_.kd
    .uniform_work_group_size: 1
    .uses_dynamic_stack: false
    .vgpr_count:     76
    .vgpr_spill_count: 0
    .wavefront_size: 64
  - .agpr_count:     4
    .args:
      - .actual_access:  read_only
        .address_space:  global
        .offset:         0
        .size:           8
        .value_kind:     global_buffer
      - .actual_access:  read_only
        .address_space:  global
        .offset:         8
        .size:           8
        .value_kind:     global_buffer
      - .actual_access:  read_only
        .address_space:  global
        .offset:         16
        .size:           8
        .value_kind:     global_buffer
      - .actual_access:  read_only
        .address_space:  global
        .offset:         24
        .size:           8
        .value_kind:     global_buffer
      - .actual_access:  read_only
        .address_space:  global
        .offset:         32
        .size:           8
        .value_kind:     global_buffer
      - .actual_access:  read_only
        .address_space:  global
        .offset:         40
        .size:           8
        .value_kind:     global_buffer
      - .actual_access:  write_only
        .address_space:  global
        .offset:         48
        .size:           8
        .value_kind:     global_buffer
      - .actual_access:  read_only
        .address_space:  global
        .offset:         56
        .size:           8
        .value_kind:     global_buffer
    .group_segment_fixed_size: 9344
    .kernarg_segment_align: 8
    .kernarg_segment_size: 64
    .language:       OpenCL C
    .language_version:
      - 2
      - 0
    .max_flat_workgroup_size: 256
    .name:           _Z5k_aggILi1EEvPKDF16_PKiPKjPKfS7_S1_PDF16_Pf
    .private_segment_fixed_size: 0
    .sgpr_count:     19
    .sgpr_spill_count: 0
    .symbol:         _Z5k_aggILi1EEvPKDF16_PKiPKjPKfS7_S1_PDF16_Pf.kd
    .uniform_work_group_size: 1
    .uses_dynamic_stack: false
    .vgpr_count:     52
    .vgpr_spill_count: 0
    .wavefront_size: 64
  - .agpr_count:     0
    .args:
      - .actual_access:  read_only
        .address_space:  global
        .offset:         0
        .size:           8
        .value_kind:     global_buffer
      - .actual_access:  read_only
        .address_space:  global
        .offset:         8
        .size:           8
        .value_kind:     global_buffer
      - .actual_access:  read_only
        .address_space:  global
        .offset:         16
        .size:           8
        .value_kind:     global_buffer
      - .actual_access:  read_only
        .address_space:  global
        .offset:         24
        .size:           8
        .value_kind:     global_buffer
      - .actual_access:  read_only
        .address_space:  global
        .offset:         32
        .size:           8
        .value_kind:     global_buffer
      - .actual_access:  read_only
        .address_space:  global
        .offset:         40
        .size:           8
        .value_kind:     global_buffer
      - .actual_access:  read_only
        .address_space:  global
        .offset:         48
        .size:           8
        .value_kind:     global_buffer
      - .actual_access:  write_only
        .address_space:  global
        .offset:         56
        .size:           8
        .value_kind:     global_buffer
    .group_segment_fixed_size: 0
    .kernarg_segment_align: 8
    .kernarg_segment_size: 64
    .language:       OpenCL C
    .language_version:
      - 2
      - 0
    .max_flat_workgroup_size: 256
    .name:           _Z5k_aggILi2EEvPKDF16_PKiPKjPKfS7_S1_PDF16_Pf
    .private_segment_fixed_size: 0
    .sgpr_count:     19
    .sgpr_spill_count: 0
    .symbol:         _Z5k_aggILi2EEvPKDF16_PKiPKjPKfS7_S1_PDF16_Pf.kd
    .uniform_work_group_size: 1
    .uses_dynamic_stack: false
    .vgpr_count:     47
    .vgpr_spill_count: 0
    .wavefront_size: 64
